# grid barrier: a block that is not its XCD's last arriver issues its agent-scope invalidate when it starts polling for the release (all its waves are parked), not after the release
# speedup vs baseline: 1.0168x; 1.0004x over previous
.LBB0_114:
	s_lshl_b32 s0, s0, 6
	s_add_i32 s6, s0, 0x500
	s_mov_b32 s7, 0
	s_lshl_b64 s[2:3], s[6:7], 2
	s_add_u32 s2, s36, s2
	s_addc_u32 s3, s37, s3
	v_mov_b32_e32 v1, 1
	v_mov_b64_e32 v[4:5], s[2:3]
	flat_atomic_add v1, v[4:5], v1 sc0
	v_cvt_f32_u32_e32 v3, v2
	v_sub_u32_e32 v4, 0, v2
	v_rcp_iflag_f32_e32 v3, v3
	s_nop 0
	v_mul_f32_e32 v3, 0x4f7ffffe, v3
	v_cvt_u32_f32_e32 v3, v3
	v_mul_lo_u32 v4, v4, v3
	v_mul_hi_u32 v4, v3, v4
	v_add_u32_e32 v3, v3, v4
	s_waitcnt vmcnt(0) lgkmcnt(0)
	v_mul_hi_u32 v3, v1, v3
	v_mul_lo_u32 v5, v3, v2
	v_add_u32_e32 v4, 1, v1
	v_sub_u32_e32 v1, v1, v5
	v_add_u32_e32 v6, 1, v3
	v_cmp_ge_u32_e32 vcc, v1, v2
	v_sub_u32_e32 v5, v1, v2
	s_nop 0
	v_cndmask_b32_e32 v3, v3, v6, vcc
	v_cndmask_b32_e32 v1, v1, v5, vcc
	v_add_u32_e32 v5, 1, v3
	v_cmp_ge_u32_e32 vcc, v1, v2
	s_nop 1
	v_cndmask_b32_e32 v1, v3, v5, vcc
	v_mad_u64_u32 v[2:3], s[2:3], v2, v1, v[2:3]
	v_cmp_ne_u32_e32 vcc, v4, v2
	s_and_saveexec_b64 s[2:3], vcc
	s_xor_b64 s[4:5], exec, s[2:3]
	s_cbranch_execz .LBB0_127
	buffer_inv sc1
	s_add_i32 s6, s0, 0x900
	s_lshl_b64 s[2:3], s[6:7], 2
	s_add_u32 s8, s36, s2
	s_addc_u32 s9, s37, s3
	v_mov_b64_e32 v[2:3], s[8:9]
	flat_load_dword v0, v[2:3] sc1
	s_waitcnt vmcnt(0) lgkmcnt(0)
	v_cmp_eq_u32_e32 vcc, v0, v1
	s_and_saveexec_b64 s[6:7], vcc
	s_cbranch_execz .LBB0_126
	s_mov_b32 s1, 1
	s_mov_b64 s[10:11], 0
	s_branch .LBB0_118

.LBB0_126:
	s_or_b64 exec, exec, s[6:7]
	s_waitcnt vmcnt(0) lgkmcnt(0)
	s_waitcnt vmcnt(0)

.LBB0_245:
	s_lshl_b32 s22, s34, 6
	s_add_i32 s36, s22, 0x500
	s_lshl_b64 s[0:1], s[36:37], 2
	s_add_u32 s0, s62, s0
	s_addc_u32 s1, s63, s1
	v_mov_b64_e32 v[4:5], s[0:1]
	flat_atomic_add v3, v[4:5], v205 sc0
	v_cvt_f32_u32_e32 v1, v2
	v_sub_u32_e32 v4, 0, v2
	v_rcp_iflag_f32_e32 v1, v1
	s_nop 0
	v_mul_f32_e32 v1, 0x4f7ffffe, v1
	v_cvt_u32_f32_e32 v1, v1
	v_mul_lo_u32 v4, v4, v1
	v_mul_hi_u32 v4, v1, v4
	v_add_u32_e32 v1, v1, v4
	s_waitcnt vmcnt(0) lgkmcnt(0)
	v_mul_hi_u32 v1, v3, v1
	v_mul_lo_u32 v4, v1, v2
	v_sub_u32_e32 v4, v3, v4
	v_cmp_ge_u32_e32 vcc, v4, v2
	v_add_u32_e32 v5, 1, v1
	s_nop 0
	v_cndmask_b32_e32 v1, v1, v5, vcc
	v_sub_u32_e32 v5, v4, v2
	v_cndmask_b32_e32 v4, v4, v5, vcc
	v_cmp_ge_u32_e32 vcc, v4, v2
	v_add_u32_e32 v4, 1, v1
	s_nop 0
	v_cndmask_b32_e32 v1, v1, v4, vcc
	v_add_u32_e32 v4, 1, v3
	v_mad_u64_u32 v[2:3], s[0:1], v2, v1, v[2:3]
	v_cmp_ne_u32_e32 vcc, v4, v2
	s_and_saveexec_b64 s[0:1], vcc
	s_xor_b64 s[0:1], exec, s[0:1]
	s_cbranch_execz .LBB0_258
	buffer_inv sc1
	s_add_i32 s36, s22, 0x900
	s_lshl_b64 s[4:5], s[36:37], 2
	s_add_u32 s6, s62, s4
	s_addc_u32 s7, s63, s5
	v_mov_b64_e32 v[2:3], s[6:7]
	flat_load_dword v0, v[2:3] sc1
	s_waitcnt vmcnt(0) lgkmcnt(0)
	v_cmp_eq_u32_e32 vcc, v0, v1
	s_and_saveexec_b64 s[4:5], vcc
	s_cbranch_execz .LBB0_257
	s_mov_b32 s2, 1
	s_mov_b64 s[8:9], 0
	s_branch .LBB0_249

.LBB0_257:
	s_or_b64 exec, exec, s[4:5]
	s_waitcnt vmcnt(0) lgkmcnt(0)
	s_waitcnt vmcnt(0)

.LBB0_1206:
	s_lshl_b32 s22, s34, 6
	s_add_i32 s36, s22, 0x500
	s_lshl_b64 s[0:1], s[36:37], 2
	s_add_u32 s0, s60, s0
	s_addc_u32 s1, s61, s1
	v_mov_b64_e32 v[4:5], s[0:1]
	flat_atomic_add v3, v[4:5], v205 sc0
	v_cvt_f32_u32_e32 v1, v2
	v_sub_u32_e32 v4, 0, v2
	v_rcp_iflag_f32_e32 v1, v1
	s_nop 0
	v_mul_f32_e32 v1, 0x4f7ffffe, v1
	v_cvt_u32_f32_e32 v1, v1
	v_mul_lo_u32 v4, v4, v1
	v_mul_hi_u32 v4, v1, v4
	v_add_u32_e32 v1, v1, v4
	s_waitcnt vmcnt(0) lgkmcnt(0)
	v_mul_hi_u32 v1, v3, v1
	v_mul_lo_u32 v4, v1, v2
	v_sub_u32_e32 v4, v3, v4
	v_cmp_ge_u32_e32 vcc, v4, v2
	v_add_u32_e32 v5, 1, v1
	s_nop 0
	v_cndmask_b32_e32 v1, v1, v5, vcc
	v_sub_u32_e32 v5, v4, v2
	v_cndmask_b32_e32 v4, v4, v5, vcc
	v_cmp_ge_u32_e32 vcc, v4, v2
	v_add_u32_e32 v4, 1, v1
	s_nop 0
	v_cndmask_b32_e32 v1, v1, v4, vcc
	v_add_u32_e32 v4, 1, v3
	v_mad_u64_u32 v[2:3], s[0:1], v2, v1, v[2:3]
	v_cmp_ne_u32_e32 vcc, v4, v2
	s_and_saveexec_b64 s[0:1], vcc
	s_xor_b64 s[0:1], exec, s[0:1]
	s_cbranch_execz .LBB0_1219
	buffer_inv sc1
	s_add_i32 s36, s22, 0x900
	s_lshl_b64 s[4:5], s[36:37], 2
	s_add_u32 s6, s60, s4
	s_addc_u32 s7, s61, s5
	v_mov_b64_e32 v[2:3], s[6:7]
	flat_load_dword v0, v[2:3] sc1
	s_waitcnt vmcnt(0) lgkmcnt(0)
	v_cmp_eq_u32_e32 vcc, v0, v1
	s_and_saveexec_b64 s[4:5], vcc
	s_cbranch_execz .LBB0_1218
	s_mov_b32 s2, 1
	s_mov_b64 s[8:9], 0
	s_branch .LBB0_1210
